# v3 + grid barrier: non-leader workgroups poll the cross-XCD release word (TOPGEN) directly; leader's per-XCD XGEN post removed
# speedup vs baseline: 1.0025x; 1.0025x over previous
; __device__ __forceinline__ unsigned xb_ld(unsigned* p)              { return __hip_atomic_load(p, __ATOMIC_RELAXED, __HIP_MEMORY_SCOPE_AGENT); }
; __device__ __forceinline__ unsigned xb_add(unsigned* p, unsigned v) { return __hip_atomic_fetch_add(p, v, __ATOMIC_RELAXED, __HIP_MEMORY_SCOPE_AGENT); }
; #define XB_SPIN(cond, bar) do { unsigned _sp = 0; while (cond) { __builtin_amdgcn_s_sleep(1); \
;     if ((++_sp & 255u) == 0u) { if (xb_ld(&(bar)[XB_TMO])) break; if (_sp > XB_SPIN_CAP) { atomicAdd(&(bar)[XB_TMO], 1u); break; } } } } while (0)
; __device__ __forceinline__ void xcd_barrier(const XcdBarrier& b) {
;     ...
;         unsigned nloc = b.st[0], nx = b.st[1];
;         if (nloc == 0u) { xcd_barrier_complete(bar, b.x, nloc, nx); b.st[0] = nloc; b.st[1] = nx; }
;         const unsigned old = xb_add(&bar[XB_XSUB(b.x)], 1u);
;         const unsigned gen = old / nloc;
;         if (old + 1u == (gen + 1u) * nloc) {
;             __builtin_amdgcn_fence(__ATOMIC_RELEASE, "agent");
;             asm volatile("s_waitcnt vmcnt(0)" ::: "memory");
;             const unsigned og = xb_add(&bar[XB_TOP], 1u);
;             const unsigned tg = og / nx;
;             if (og + 1u == (tg + 1u) * nx) xb_add(&bar[XB_TOPGEN], 1u);
;             else XB_SPIN(xb_ld(&bar[XB_TOPGEN]) == tg, bar);
;             __builtin_amdgcn_fence(__ATOMIC_ACQUIRE, "agent");
;             xb_add(&bar[XB_XGEN(b.x)], 1u);
;             asm volatile("s_waitcnt vmcnt(0)" ::: "memory");
;         } else {
;             XB_SPIN(xb_ld(&bar[XB_XGEN(b.x)]) == gen, bar);
.LBB0_157:
	v_readlane_b32 s4, v252, 35
	v_readlane_b32 s5, v252, 36
	s_lshl_b64 s[4:5], s[4:5], 2
	v_readlane_b32 s6, v252, 33
	s_add_u32 s8, s6, s4
	v_readlane_b32 s4, v252, 34
	s_addc_u32 s9, s4, s5
	v_readlane_b32 s4, v252, 37
	s_lshl_b32 s4, s4, 8
	s_add_u32 s6, s8, s4
	s_addc_u32 s7, s9, 0
	v_mov_b32_e32 v2, 0x1000
	v_mov_b32_e32 v4, 1
	global_atomic_add v4, v2, v4, s[6:7] offset:1024 sc0
	v_cvt_f32_u32_e32 v2, v3
	v_sub_u32_e32 v5, 0, v3
	v_rcp_iflag_f32_e32 v2, v2
	s_nop 0
	v_mul_f32_e32 v2, 0x4f7ffffe, v2
	v_cvt_u32_f32_e32 v2, v2
	v_mul_lo_u32 v5, v5, v2
	v_mul_hi_u32 v5, v2, v5
	v_add_u32_e32 v2, v2, v5
	s_waitcnt vmcnt(0)
	v_mul_hi_u32 v2, v4, v2
	v_mul_lo_u32 v5, v2, v3
	v_sub_u32_e32 v5, v4, v5
	v_add_u32_e32 v6, 1, v2
	v_cmp_ge_u32_e32 vcc, v5, v3
	v_add_u32_e32 v4, 1, v4
	s_nop 0
	v_cndmask_b32_e32 v2, v2, v6, vcc
	v_sub_u32_e32 v6, v5, v3
	v_cndmask_b32_e32 v5, v5, v6, vcc
	v_add_u32_e32 v6, 1, v2
	v_cmp_ge_u32_e32 vcc, v5, v3
	s_nop 1
	v_cndmask_b32_e32 v2, v2, v6, vcc
	v_mul_lo_u32 v5, v3, v2
	v_add_u32_e32 v3, v5, v3
	v_cmp_ne_u32_e32 vcc, v4, v3
	s_and_saveexec_b64 s[4:5], vcc
	s_xor_b64 s[10:11], exec, s[4:5]
	s_cbranch_execz .LBB0_171
	s_waitcnt lgkmcnt(0)
	v_mov_b32_e32 v1, 0x3000
	global_load_dword v1, v1, s[8:9] offset:1280 sc1
	s_add_u32 s14, s8, 0x3500
	s_addc_u32 s15, s9, 0
	s_waitcnt vmcnt(0)
	v_cmp_eq_u32_e32 vcc, v1, v2
	s_and_saveexec_b64 s[12:13], vcc
	s_cbranch_execz .LBB0_170
	s_mov_b32 s24, 1
	s_mov_b64 s[16:17], 0
	v_mov_b32_e32 v1, 0
	s_branch .LBB0_161

; __device__ __forceinline__ unsigned xb_ld(unsigned* p)              { return __hip_atomic_load(p, __ATOMIC_RELAXED, __HIP_MEMORY_SCOPE_AGENT); }
; __device__ __forceinline__ unsigned xb_add(unsigned* p, unsigned v) { return __hip_atomic_fetch_add(p, v, __ATOMIC_RELAXED, __HIP_MEMORY_SCOPE_AGENT); }
; #define XB_SPIN(cond, bar) do { unsigned _sp = 0; while (cond) { __builtin_amdgcn_s_sleep(1); \
;     if ((++_sp & 255u) == 0u) { if (xb_ld(&(bar)[XB_TMO])) break; if (_sp > XB_SPIN_CAP) { atomicAdd(&(bar)[XB_TMO], 1u); break; } } } } while (0)
; __device__ __forceinline__ void xcd_barrier(const XcdBarrier& b) {
;     ...
;         if (old + 1u == (gen + 1u) * nloc) {
;             __builtin_amdgcn_fence(__ATOMIC_RELEASE, "agent");
;             asm volatile("s_waitcnt vmcnt(0)" ::: "memory");
;             const unsigned og = xb_add(&bar[XB_TOP], 1u);
;             const unsigned tg = og / nx;
;             if (og + 1u == (tg + 1u) * nx) xb_add(&bar[XB_TOPGEN], 1u);
;             else XB_SPIN(xb_ld(&bar[XB_TOPGEN]) == tg, bar);
;             __builtin_amdgcn_fence(__ATOMIC_ACQUIRE, "agent");
;             xb_add(&bar[XB_XGEN(b.x)], 1u);
;             asm volatile("s_waitcnt vmcnt(0)" ::: "memory");
.LBB0_188:
	s_or_b64 exec, exec, s[8:9]
	v_mov_b32_e32 v1, 0x2000
	v_mov_b32_e32 v2, 1
	s_waitcnt vmcnt(0)
	buffer_inv sc1
	s_waitcnt vmcnt(0)

; __device__ __forceinline__ unsigned xb_ld(unsigned* p)              { return __hip_atomic_load(p, __ATOMIC_RELAXED, __HIP_MEMORY_SCOPE_AGENT); }
; __device__ __forceinline__ unsigned xb_add(unsigned* p, unsigned v) { return __hip_atomic_fetch_add(p, v, __ATOMIC_RELAXED, __HIP_MEMORY_SCOPE_AGENT); }
; #define XB_SPIN(cond, bar) do { unsigned _sp = 0; while (cond) { __builtin_amdgcn_s_sleep(1); \
;     if ((++_sp & 255u) == 0u) { if (xb_ld(&(bar)[XB_TMO])) break; if (_sp > XB_SPIN_CAP) { atomicAdd(&(bar)[XB_TMO], 1u); break; } } } } while (0)
; __device__ __forceinline__ void xcd_barrier(const XcdBarrier& b) {
;     ...
;         unsigned nloc = b.st[0], nx = b.st[1];
;         if (nloc == 0u) { xcd_barrier_complete(bar, b.x, nloc, nx); b.st[0] = nloc; b.st[1] = nx; }
;         const unsigned old = xb_add(&bar[XB_XSUB(b.x)], 1u);
;         const unsigned gen = old / nloc;
;         if (old + 1u == (gen + 1u) * nloc) {
;             __builtin_amdgcn_fence(__ATOMIC_RELEASE, "agent");
;             asm volatile("s_waitcnt vmcnt(0)" ::: "memory");
;             const unsigned og = xb_add(&bar[XB_TOP], 1u);
;             const unsigned tg = og / nx;
;             if (og + 1u == (tg + 1u) * nx) xb_add(&bar[XB_TOPGEN], 1u);
;             else XB_SPIN(xb_ld(&bar[XB_TOPGEN]) == tg, bar);
;             __builtin_amdgcn_fence(__ATOMIC_ACQUIRE, "agent");
;             xb_add(&bar[XB_XGEN(b.x)], 1u);
;             asm volatile("s_waitcnt vmcnt(0)" ::: "memory");
;         } else {
;             XB_SPIN(xb_ld(&bar[XB_XGEN(b.x)]) == gen, bar);
.LBB0_231:
	v_readlane_b32 s4, v252, 35
	v_readlane_b32 s5, v252, 36
	s_lshl_b64 s[4:5], s[4:5], 2
	v_readlane_b32 s6, v252, 33
	s_add_u32 s6, s6, s4
	v_readlane_b32 s4, v252, 34
	s_addc_u32 s7, s4, s5
	v_readlane_b32 s4, v252, 37
	s_lshl_b32 s4, s4, 8
	s_add_u32 s4, s6, s4
	s_addc_u32 s5, s7, 0
	v_mov_b32_e32 v2, 0x1000
	v_mov_b32_e32 v4, 1
	global_atomic_add v4, v2, v4, s[4:5] offset:1024 sc0
	v_cvt_f32_u32_e32 v2, v3
	v_sub_u32_e32 v5, 0, v3
	v_rcp_iflag_f32_e32 v2, v2
	s_nop 0
	v_mul_f32_e32 v2, 0x4f7ffffe, v2
	v_cvt_u32_f32_e32 v2, v2
	v_mul_lo_u32 v5, v5, v2
	v_mul_hi_u32 v5, v2, v5
	v_add_u32_e32 v2, v2, v5
	s_waitcnt vmcnt(0)
	v_mul_hi_u32 v2, v4, v2
	v_mul_lo_u32 v5, v2, v3
	v_sub_u32_e32 v5, v4, v5
	v_add_u32_e32 v6, 1, v2
	v_cmp_ge_u32_e32 vcc, v5, v3
	v_add_u32_e32 v4, 1, v4
	s_nop 0
	v_cndmask_b32_e32 v2, v2, v6, vcc
	v_sub_u32_e32 v6, v5, v3
	v_cndmask_b32_e32 v5, v5, v6, vcc
	v_add_u32_e32 v6, 1, v2
	v_cmp_ge_u32_e32 vcc, v5, v3
	s_nop 1
	v_cndmask_b32_e32 v2, v2, v6, vcc
	v_mul_lo_u32 v5, v3, v2
	v_add_u32_e32 v3, v5, v3
	v_cmp_ne_u32_e32 vcc, v4, v3
	s_and_saveexec_b64 s[8:9], vcc
	s_xor_b64 s[8:9], exec, s[8:9]
	s_cbranch_execz .LBB0_245
	s_waitcnt lgkmcnt(0)
	v_mov_b32_e32 v1, 0x3000
	global_load_dword v1, v1, s[6:7] offset:1280 sc1
	s_add_u32 s16, s6, 0x3500
	s_addc_u32 s17, s7, 0
	s_waitcnt vmcnt(0)
	v_cmp_eq_u32_e32 vcc, v1, v2
	s_and_saveexec_b64 s[14:15], vcc
	s_cbranch_execz .LBB0_244
	s_mov_b32 s28, 1
	s_mov_b64 s[18:19], 0
	v_mov_b32_e32 v1, 0
	s_branch .LBB0_235

; __device__ __forceinline__ unsigned xb_ld(unsigned* p)              { return __hip_atomic_load(p, __ATOMIC_RELAXED, __HIP_MEMORY_SCOPE_AGENT); }
; __device__ __forceinline__ unsigned xb_add(unsigned* p, unsigned v) { return __hip_atomic_fetch_add(p, v, __ATOMIC_RELAXED, __HIP_MEMORY_SCOPE_AGENT); }
; #define XB_SPIN(cond, bar) do { unsigned _sp = 0; while (cond) { __builtin_amdgcn_s_sleep(1); \
;     if ((++_sp & 255u) == 0u) { if (xb_ld(&(bar)[XB_TMO])) break; if (_sp > XB_SPIN_CAP) { atomicAdd(&(bar)[XB_TMO], 1u); break; } } } } while (0)
; __device__ __forceinline__ void xcd_barrier(const XcdBarrier& b) {
;     ...
;         if (old + 1u == (gen + 1u) * nloc) {
;             __builtin_amdgcn_fence(__ATOMIC_RELEASE, "agent");
;             asm volatile("s_waitcnt vmcnt(0)" ::: "memory");
;             const unsigned og = xb_add(&bar[XB_TOP], 1u);
;             const unsigned tg = og / nx;
;             if (og + 1u == (tg + 1u) * nx) xb_add(&bar[XB_TOPGEN], 1u);
;             else XB_SPIN(xb_ld(&bar[XB_TOPGEN]) == tg, bar);
;             __builtin_amdgcn_fence(__ATOMIC_ACQUIRE, "agent");
;             xb_add(&bar[XB_XGEN(b.x)], 1u);
;             asm volatile("s_waitcnt vmcnt(0)" ::: "memory");
.LBB0_262:
	s_or_b64 exec, exec, s[6:7]
	v_mov_b32_e32 v1, 0x2000
	v_mov_b32_e32 v2, 1
	s_waitcnt vmcnt(0)
	buffer_inv sc1
	s_waitcnt vmcnt(0)

; __device__ __forceinline__ unsigned xb_ld(unsigned* p)              { return __hip_atomic_load(p, __ATOMIC_RELAXED, __HIP_MEMORY_SCOPE_AGENT); }
; __device__ __forceinline__ unsigned xb_add(unsigned* p, unsigned v) { return __hip_atomic_fetch_add(p, v, __ATOMIC_RELAXED, __HIP_MEMORY_SCOPE_AGENT); }
; #define XB_SPIN(cond, bar) do { unsigned _sp = 0; while (cond) { __builtin_amdgcn_s_sleep(1); \
;     if ((++_sp & 255u) == 0u) { if (xb_ld(&(bar)[XB_TMO])) break; if (_sp > XB_SPIN_CAP) { atomicAdd(&(bar)[XB_TMO], 1u); break; } } } } while (0)
; __device__ __forceinline__ void xcd_barrier(const XcdBarrier& b) {
;     ...
;         unsigned nloc = b.st[0], nx = b.st[1];
;         if (nloc == 0u) { xcd_barrier_complete(bar, b.x, nloc, nx); b.st[0] = nloc; b.st[1] = nx; }
;         const unsigned old = xb_add(&bar[XB_XSUB(b.x)], 1u);
;         const unsigned gen = old / nloc;
;         if (old + 1u == (gen + 1u) * nloc) {
;             __builtin_amdgcn_fence(__ATOMIC_RELEASE, "agent");
;             asm volatile("s_waitcnt vmcnt(0)" ::: "memory");
;             const unsigned og = xb_add(&bar[XB_TOP], 1u);
;             const unsigned tg = og / nx;
;             if (og + 1u == (tg + 1u) * nx) xb_add(&bar[XB_TOPGEN], 1u);
;             else XB_SPIN(xb_ld(&bar[XB_TOPGEN]) == tg, bar);
;             __builtin_amdgcn_fence(__ATOMIC_ACQUIRE, "agent");
;             xb_add(&bar[XB_XGEN(b.x)], 1u);
;             asm volatile("s_waitcnt vmcnt(0)" ::: "memory");
;         } else {
;             XB_SPIN(xb_ld(&bar[XB_XGEN(b.x)]) == gen, bar);
.LBB0_390:
	v_readlane_b32 s4, v252, 35
	v_readlane_b32 s5, v252, 36
	s_lshl_b64 s[4:5], s[4:5], 2
	v_readlane_b32 s6, v252, 33
	s_add_u32 s6, s6, s4
	v_readlane_b32 s4, v252, 34
	s_addc_u32 s7, s4, s5
	v_readlane_b32 s4, v252, 37
	s_lshl_b32 s4, s4, 8
	s_add_u32 s4, s6, s4
	s_addc_u32 s5, s7, 0
	v_mov_b32_e32 v2, 0x1000
	v_mov_b32_e32 v4, 1
	global_atomic_add v4, v2, v4, s[4:5] offset:1024 sc0
	v_cvt_f32_u32_e32 v2, v3
	v_sub_u32_e32 v5, 0, v3
	v_rcp_iflag_f32_e32 v2, v2
	s_nop 0
	v_mul_f32_e32 v2, 0x4f7ffffe, v2
	v_cvt_u32_f32_e32 v2, v2
	v_mul_lo_u32 v5, v5, v2
	v_mul_hi_u32 v5, v2, v5
	v_add_u32_e32 v2, v2, v5
	s_waitcnt vmcnt(0)
	v_mul_hi_u32 v2, v4, v2
	v_mul_lo_u32 v5, v2, v3
	v_sub_u32_e32 v5, v4, v5
	v_add_u32_e32 v6, 1, v2
	v_cmp_ge_u32_e32 vcc, v5, v3
	v_add_u32_e32 v4, 1, v4
	s_nop 0
	v_cndmask_b32_e32 v2, v2, v6, vcc
	v_sub_u32_e32 v6, v5, v3
	v_cndmask_b32_e32 v5, v5, v6, vcc
	v_add_u32_e32 v6, 1, v2
	v_cmp_ge_u32_e32 vcc, v5, v3
	s_nop 1
	v_cndmask_b32_e32 v2, v2, v6, vcc
	v_mul_lo_u32 v5, v3, v2
	v_add_u32_e32 v3, v5, v3
	v_cmp_ne_u32_e32 vcc, v4, v3
	s_and_saveexec_b64 s[8:9], vcc
	s_xor_b64 s[8:9], exec, s[8:9]
	s_cbranch_execz .LBB0_404
	s_waitcnt lgkmcnt(0)
	v_mov_b32_e32 v1, 0x3000
	global_load_dword v1, v1, s[6:7] offset:1280 sc1
	s_add_u32 s12, s6, 0x3500
	s_addc_u32 s13, s7, 0
	s_waitcnt vmcnt(0)
	v_cmp_eq_u32_e32 vcc, v1, v2
	s_and_saveexec_b64 s[10:11], vcc
	s_cbranch_execz .LBB0_403
	s_mov_b32 s24, 1
	s_mov_b64 s[14:15], 0
	v_mov_b32_e32 v1, 0
	s_branch .LBB0_394

; __device__ __forceinline__ unsigned xb_ld(unsigned* p)              { return __hip_atomic_load(p, __ATOMIC_RELAXED, __HIP_MEMORY_SCOPE_AGENT); }
; __device__ __forceinline__ unsigned xb_add(unsigned* p, unsigned v) { return __hip_atomic_fetch_add(p, v, __ATOMIC_RELAXED, __HIP_MEMORY_SCOPE_AGENT); }
; #define XB_SPIN(cond, bar) do { unsigned _sp = 0; while (cond) { __builtin_amdgcn_s_sleep(1); \
;     if ((++_sp & 255u) == 0u) { if (xb_ld(&(bar)[XB_TMO])) break; if (_sp > XB_SPIN_CAP) { atomicAdd(&(bar)[XB_TMO], 1u); break; } } } } while (0)
; __device__ __forceinline__ void xcd_barrier(const XcdBarrier& b) {
;     ...
;         unsigned nloc = b.st[0], nx = b.st[1];
;         if (nloc == 0u) { xcd_barrier_complete(bar, b.x, nloc, nx); b.st[0] = nloc; b.st[1] = nx; }
;         const unsigned old = xb_add(&bar[XB_XSUB(b.x)], 1u);
;         const unsigned gen = old / nloc;
;         if (old + 1u == (gen + 1u) * nloc) {
;             __builtin_amdgcn_fence(__ATOMIC_RELEASE, "agent");
;             asm volatile("s_waitcnt vmcnt(0)" ::: "memory");
;             const unsigned og = xb_add(&bar[XB_TOP], 1u);
;             const unsigned tg = og / nx;
;             if (og + 1u == (tg + 1u) * nx) xb_add(&bar[XB_TOPGEN], 1u);
;             else XB_SPIN(xb_ld(&bar[XB_TOPGEN]) == tg, bar);
;             __builtin_amdgcn_fence(__ATOMIC_ACQUIRE, "agent");
;             xb_add(&bar[XB_XGEN(b.x)], 1u);
;             asm volatile("s_waitcnt vmcnt(0)" ::: "memory");
;         } else {
;             XB_SPIN(xb_ld(&bar[XB_XGEN(b.x)]) == gen, bar);
.LBB0_775:
	v_readlane_b32 s4, v252, 35
	v_readlane_b32 s5, v252, 36
	s_lshl_b64 s[4:5], s[4:5], 2
	v_readlane_b32 s6, v252, 33
	s_add_u32 s6, s6, s4
	v_readlane_b32 s4, v252, 34
	s_addc_u32 s7, s4, s5
	v_readlane_b32 s4, v252, 37
	s_lshl_b32 s4, s4, 8
	s_add_u32 s4, s6, s4
	s_addc_u32 s5, s7, 0
	v_mov_b32_e32 v2, 0x1000
	v_mov_b32_e32 v4, 1
	global_atomic_add v4, v2, v4, s[4:5] offset:1024 sc0
	v_cvt_f32_u32_e32 v2, v3
	v_sub_u32_e32 v5, 0, v3
	v_rcp_iflag_f32_e32 v2, v2
	s_nop 0
	v_mul_f32_e32 v2, 0x4f7ffffe, v2
	v_cvt_u32_f32_e32 v2, v2
	v_mul_lo_u32 v5, v5, v2
	v_mul_hi_u32 v5, v2, v5
	v_add_u32_e32 v2, v2, v5
	s_waitcnt vmcnt(0)
	v_mul_hi_u32 v2, v4, v2
	v_mul_lo_u32 v5, v2, v3
	v_sub_u32_e32 v5, v4, v5
	v_add_u32_e32 v6, 1, v2
	v_cmp_ge_u32_e32 vcc, v5, v3
	v_add_u32_e32 v4, 1, v4
	s_nop 0
	v_cndmask_b32_e32 v2, v2, v6, vcc
	v_sub_u32_e32 v6, v5, v3
	v_cndmask_b32_e32 v5, v5, v6, vcc
	v_add_u32_e32 v6, 1, v2
	v_cmp_ge_u32_e32 vcc, v5, v3
	s_nop 1
	v_cndmask_b32_e32 v2, v2, v6, vcc
	v_mul_lo_u32 v5, v3, v2
	v_add_u32_e32 v3, v5, v3
	v_cmp_ne_u32_e32 vcc, v4, v3
	s_and_saveexec_b64 s[8:9], vcc
	s_xor_b64 s[8:9], exec, s[8:9]
	s_cbranch_execz .LBB0_789
	s_waitcnt lgkmcnt(0)
	v_mov_b32_e32 v1, 0x3000
	global_load_dword v1, v1, s[6:7] offset:1280 sc1
	s_add_u32 s12, s6, 0x3500
	s_addc_u32 s13, s7, 0
	s_waitcnt vmcnt(0)
	v_cmp_eq_u32_e32 vcc, v1, v2
	s_and_saveexec_b64 s[10:11], vcc
	s_cbranch_execz .LBB0_788
	s_mov_b32 s33, 1
	s_mov_b64 s[14:15], 0
	v_mov_b32_e32 v1, 0
	s_branch .LBB0_779

; __device__ __forceinline__ unsigned xb_ld(unsigned* p)              { return __hip_atomic_load(p, __ATOMIC_RELAXED, __HIP_MEMORY_SCOPE_AGENT); }
; __device__ __forceinline__ unsigned xb_add(unsigned* p, unsigned v) { return __hip_atomic_fetch_add(p, v, __ATOMIC_RELAXED, __HIP_MEMORY_SCOPE_AGENT); }
; #define XB_SPIN(cond, bar) do { unsigned _sp = 0; while (cond) { __builtin_amdgcn_s_sleep(1); \
;     if ((++_sp & 255u) == 0u) { if (xb_ld(&(bar)[XB_TMO])) break; if (_sp > XB_SPIN_CAP) { atomicAdd(&(bar)[XB_TMO], 1u); break; } } } } while (0)
; __device__ __forceinline__ void xcd_barrier(const XcdBarrier& b) {
;     ...
;         unsigned nloc = b.st[0], nx = b.st[1];
;         if (nloc == 0u) { xcd_barrier_complete(bar, b.x, nloc, nx); b.st[0] = nloc; b.st[1] = nx; }
;         const unsigned old = xb_add(&bar[XB_XSUB(b.x)], 1u);
;         const unsigned gen = old / nloc;
;         if (old + 1u == (gen + 1u) * nloc) {
;             __builtin_amdgcn_fence(__ATOMIC_RELEASE, "agent");
;             asm volatile("s_waitcnt vmcnt(0)" ::: "memory");
;             const unsigned og = xb_add(&bar[XB_TOP], 1u);
;             const unsigned tg = og / nx;
;             if (og + 1u == (tg + 1u) * nx) xb_add(&bar[XB_TOPGEN], 1u);
;             else XB_SPIN(xb_ld(&bar[XB_TOPGEN]) == tg, bar);
;             __builtin_amdgcn_fence(__ATOMIC_ACQUIRE, "agent");
;             xb_add(&bar[XB_XGEN(b.x)], 1u);
;             asm volatile("s_waitcnt vmcnt(0)" ::: "memory");
;         } else {
;             XB_SPIN(xb_ld(&bar[XB_XGEN(b.x)]) == gen, bar);
.LBB0_924:
	v_readlane_b32 s2, v252, 35
	v_readlane_b32 s3, v252, 36
	s_lshl_b64 s[2:3], s[2:3], 2
	v_readlane_b32 s10, v252, 33
	s_add_u32 s10, s10, s2
	v_readlane_b32 s2, v252, 34
	s_addc_u32 s11, s2, s3
	v_readlane_b32 s2, v252, 37
	s_lshl_b32 s2, s2, 8
	s_add_u32 s2, s10, s2
	s_addc_u32 s3, s11, 0
	v_mov_b32_e32 v2, 0x1000
	v_mov_b32_e32 v4, 1
	global_atomic_add v4, v2, v4, s[2:3] offset:1024 sc0
	v_cvt_f32_u32_e32 v2, v3
	v_sub_u32_e32 v5, 0, v3
	v_rcp_iflag_f32_e32 v2, v2
	s_nop 0
	v_mul_f32_e32 v2, 0x4f7ffffe, v2
	v_cvt_u32_f32_e32 v2, v2
	v_mul_lo_u32 v5, v5, v2
	v_mul_hi_u32 v5, v2, v5
	v_add_u32_e32 v2, v2, v5
	s_waitcnt vmcnt(0)
	v_mul_hi_u32 v2, v4, v2
	v_mul_lo_u32 v5, v2, v3
	v_sub_u32_e32 v5, v4, v5
	v_add_u32_e32 v6, 1, v2
	v_cmp_ge_u32_e32 vcc, v5, v3
	v_add_u32_e32 v4, 1, v4
	s_nop 0
	v_cndmask_b32_e32 v2, v2, v6, vcc
	v_sub_u32_e32 v6, v5, v3
	v_cndmask_b32_e32 v5, v5, v6, vcc
	v_add_u32_e32 v6, 1, v2
	v_cmp_ge_u32_e32 vcc, v5, v3
	s_nop 1
	v_cndmask_b32_e32 v2, v2, v6, vcc
	v_mul_lo_u32 v5, v3, v2
	v_add_u32_e32 v3, v5, v3
	v_cmp_ne_u32_e32 vcc, v4, v3
	s_and_saveexec_b64 s[12:13], vcc
	s_xor_b64 s[12:13], exec, s[12:13]
	s_cbranch_execz .LBB0_938
	s_waitcnt lgkmcnt(0)
	v_mov_b32_e32 v1, 0x3000
	global_load_dword v1, v1, s[10:11] offset:1280 sc1
	s_add_u32 s16, s10, 0x3500
	s_addc_u32 s17, s11, 0
	s_waitcnt vmcnt(0)
	v_cmp_eq_u32_e32 vcc, v1, v2
	s_and_saveexec_b64 s[14:15], vcc
	s_cbranch_execz .LBB0_937
	s_mov_b32 s33, 1
	s_mov_b64 s[28:29], 0
	v_mov_b32_e32 v1, 0
	s_branch .LBB0_928

; __device__ __forceinline__ unsigned xb_ld(unsigned* p)              { return __hip_atomic_load(p, __ATOMIC_RELAXED, __HIP_MEMORY_SCOPE_AGENT); }
; __device__ __forceinline__ unsigned xb_add(unsigned* p, unsigned v) { return __hip_atomic_fetch_add(p, v, __ATOMIC_RELAXED, __HIP_MEMORY_SCOPE_AGENT); }
; #define XB_SPIN(cond, bar) do { unsigned _sp = 0; while (cond) { __builtin_amdgcn_s_sleep(1); \
;     if ((++_sp & 255u) == 0u) { if (xb_ld(&(bar)[XB_TMO])) break; if (_sp > XB_SPIN_CAP) { atomicAdd(&(bar)[XB_TMO], 1u); break; } } } } while (0)
; __device__ __forceinline__ void xcd_barrier(const XcdBarrier& b) {
;     ...
;         if (old + 1u == (gen + 1u) * nloc) {
;             __builtin_amdgcn_fence(__ATOMIC_RELEASE, "agent");
;             asm volatile("s_waitcnt vmcnt(0)" ::: "memory");
;             const unsigned og = xb_add(&bar[XB_TOP], 1u);
;             const unsigned tg = og / nx;
;             if (og + 1u == (tg + 1u) * nx) xb_add(&bar[XB_TOPGEN], 1u);
;             else XB_SPIN(xb_ld(&bar[XB_TOPGEN]) == tg, bar);
;             __builtin_amdgcn_fence(__ATOMIC_ACQUIRE, "agent");
;             xb_add(&bar[XB_XGEN(b.x)], 1u);
;             asm volatile("s_waitcnt vmcnt(0)" ::: "memory");
.LBB0_955:
	s_or_b64 exec, exec, s[10:11]
	v_mov_b32_e32 v1, 0x2000
	v_mov_b32_e32 v2, 1
	s_waitcnt vmcnt(0)
	buffer_inv sc1
	s_waitcnt vmcnt(0)

; __device__ __forceinline__ unsigned xb_ld(unsigned* p)              { return __hip_atomic_load(p, __ATOMIC_RELAXED, __HIP_MEMORY_SCOPE_AGENT); }
; __device__ __forceinline__ unsigned xb_add(unsigned* p, unsigned v) { return __hip_atomic_fetch_add(p, v, __ATOMIC_RELAXED, __HIP_MEMORY_SCOPE_AGENT); }
; #define XB_SPIN(cond, bar) do { unsigned _sp = 0; while (cond) { __builtin_amdgcn_s_sleep(1); \
;     if ((++_sp & 255u) == 0u) { if (xb_ld(&(bar)[XB_TMO])) break; if (_sp > XB_SPIN_CAP) { atomicAdd(&(bar)[XB_TMO], 1u); break; } } } } while (0)
; __device__ __forceinline__ void xcd_barrier(const XcdBarrier& b) {
;     ...
;         unsigned nloc = b.st[0], nx = b.st[1];
;         if (nloc == 0u) { xcd_barrier_complete(bar, b.x, nloc, nx); b.st[0] = nloc; b.st[1] = nx; }
;         const unsigned old = xb_add(&bar[XB_XSUB(b.x)], 1u);
;         const unsigned gen = old / nloc;
;         if (old + 1u == (gen + 1u) * nloc) {
;             __builtin_amdgcn_fence(__ATOMIC_RELEASE, "agent");
;             asm volatile("s_waitcnt vmcnt(0)" ::: "memory");
;             const unsigned og = xb_add(&bar[XB_TOP], 1u);
;             const unsigned tg = og / nx;
;             if (og + 1u == (tg + 1u) * nx) xb_add(&bar[XB_TOPGEN], 1u);
;             else XB_SPIN(xb_ld(&bar[XB_TOPGEN]) == tg, bar);
;             __builtin_amdgcn_fence(__ATOMIC_ACQUIRE, "agent");
;             xb_add(&bar[XB_XGEN(b.x)], 1u);
;             asm volatile("s_waitcnt vmcnt(0)" ::: "memory");
;         } else {
;             XB_SPIN(xb_ld(&bar[XB_XGEN(b.x)]) == gen, bar);
.LBB0_998:
	v_readlane_b32 s4, v252, 35
	v_readlane_b32 s5, v252, 36
	s_lshl_b64 s[4:5], s[4:5], 2
	v_readlane_b32 s6, v252, 33
	s_add_u32 s6, s6, s4
	v_readlane_b32 s4, v252, 34
	s_addc_u32 s7, s4, s5
	v_readlane_b32 s4, v252, 37
	s_lshl_b32 s4, s4, 8
	s_add_u32 s4, s6, s4
	s_addc_u32 s5, s7, 0
	v_mov_b32_e32 v2, 0x1000
	v_mov_b32_e32 v4, 1
	global_atomic_add v4, v2, v4, s[4:5] offset:1024 sc0
	v_cvt_f32_u32_e32 v2, v3
	v_sub_u32_e32 v5, 0, v3
	v_rcp_iflag_f32_e32 v2, v2
	s_nop 0
	v_mul_f32_e32 v2, 0x4f7ffffe, v2
	v_cvt_u32_f32_e32 v2, v2
	v_mul_lo_u32 v5, v5, v2
	v_mul_hi_u32 v5, v2, v5
	v_add_u32_e32 v2, v2, v5
	s_waitcnt vmcnt(0)
	v_mul_hi_u32 v2, v4, v2
	v_mul_lo_u32 v5, v2, v3
	v_sub_u32_e32 v5, v4, v5
	v_add_u32_e32 v6, 1, v2
	v_cmp_ge_u32_e32 vcc, v5, v3
	v_add_u32_e32 v4, 1, v4
	s_nop 0
	v_cndmask_b32_e32 v2, v2, v6, vcc
	v_sub_u32_e32 v6, v5, v3
	v_cndmask_b32_e32 v5, v5, v6, vcc
	v_add_u32_e32 v6, 1, v2
	v_cmp_ge_u32_e32 vcc, v5, v3
	s_nop 1
	v_cndmask_b32_e32 v2, v2, v6, vcc
	v_mul_lo_u32 v5, v3, v2
	v_add_u32_e32 v3, v5, v3
	v_cmp_ne_u32_e32 vcc, v4, v3
	s_and_saveexec_b64 s[8:9], vcc
	s_xor_b64 s[8:9], exec, s[8:9]
	s_cbranch_execz .LBB0_1012
	s_waitcnt lgkmcnt(0)
	v_mov_b32_e32 v1, 0x3000
	global_load_dword v1, v1, s[6:7] offset:1280 sc1
	s_add_u32 s12, s6, 0x3500
	s_addc_u32 s13, s7, 0
	s_waitcnt vmcnt(0)
	v_cmp_eq_u32_e32 vcc, v1, v2
	s_and_saveexec_b64 s[10:11], vcc
	s_cbranch_execz .LBB0_1011
	s_mov_b32 s30, 1
	s_mov_b64 s[14:15], 0
	v_mov_b32_e32 v1, 0
	s_branch .LBB0_1002

; __device__ __forceinline__ unsigned xb_ld(unsigned* p)              { return __hip_atomic_load(p, __ATOMIC_RELAXED, __HIP_MEMORY_SCOPE_AGENT); }
; __device__ __forceinline__ unsigned xb_add(unsigned* p, unsigned v) { return __hip_atomic_fetch_add(p, v, __ATOMIC_RELAXED, __HIP_MEMORY_SCOPE_AGENT); }
; #define XB_SPIN(cond, bar) do { unsigned _sp = 0; while (cond) { __builtin_amdgcn_s_sleep(1); \
;     if ((++_sp & 255u) == 0u) { if (xb_ld(&(bar)[XB_TMO])) break; if (_sp > XB_SPIN_CAP) { atomicAdd(&(bar)[XB_TMO], 1u); break; } } } } while (0)
; __device__ __forceinline__ void xcd_barrier(const XcdBarrier& b) {
;     ...
;         unsigned nloc = b.st[0], nx = b.st[1];
;         if (nloc == 0u) { xcd_barrier_complete(bar, b.x, nloc, nx); b.st[0] = nloc; b.st[1] = nx; }
;         const unsigned old = xb_add(&bar[XB_XSUB(b.x)], 1u);
;         const unsigned gen = old / nloc;
;         if (old + 1u == (gen + 1u) * nloc) {
;             __builtin_amdgcn_fence(__ATOMIC_RELEASE, "agent");
;             asm volatile("s_waitcnt vmcnt(0)" ::: "memory");
;             const unsigned og = xb_add(&bar[XB_TOP], 1u);
;             const unsigned tg = og / nx;
;             if (og + 1u == (tg + 1u) * nx) xb_add(&bar[XB_TOPGEN], 1u);
;             else XB_SPIN(xb_ld(&bar[XB_TOPGEN]) == tg, bar);
;             __builtin_amdgcn_fence(__ATOMIC_ACQUIRE, "agent");
;             xb_add(&bar[XB_XGEN(b.x)], 1u);
;             asm volatile("s_waitcnt vmcnt(0)" ::: "memory");
;         } else {
;             XB_SPIN(xb_ld(&bar[XB_XGEN(b.x)]) == gen, bar);
.LBB0_1060:
	v_readlane_b32 s2, v252, 35
	v_readlane_b32 s3, v252, 36
	s_lshl_b64 s[2:3], s[2:3], 2
	v_readlane_b32 s4, v252, 33
	s_add_u32 s4, s4, s2
	v_readlane_b32 s2, v252, 34
	s_addc_u32 s5, s2, s3
	v_readlane_b32 s2, v252, 37
	s_lshl_b32 s2, s2, 8
	s_add_u32 s2, s4, s2
	s_addc_u32 s3, s5, 0
	v_mov_b32_e32 v2, 0x1000
	v_mov_b32_e32 v4, 1
	global_atomic_add v4, v2, v4, s[2:3] offset:1024 sc0
	v_cvt_f32_u32_e32 v2, v3
	v_sub_u32_e32 v5, 0, v3
	v_rcp_iflag_f32_e32 v2, v2
	s_nop 0
	v_mul_f32_e32 v2, 0x4f7ffffe, v2
	v_cvt_u32_f32_e32 v2, v2
	v_mul_lo_u32 v5, v5, v2
	v_mul_hi_u32 v5, v2, v5
	v_add_u32_e32 v2, v2, v5
	s_waitcnt vmcnt(0)
	v_mul_hi_u32 v2, v4, v2
	v_mul_lo_u32 v5, v2, v3
	v_sub_u32_e32 v5, v4, v5
	v_add_u32_e32 v6, 1, v2
	v_cmp_ge_u32_e32 vcc, v5, v3
	v_add_u32_e32 v4, 1, v4
	s_nop 0
	v_cndmask_b32_e32 v2, v2, v6, vcc
	v_sub_u32_e32 v6, v5, v3
	v_cndmask_b32_e32 v5, v5, v6, vcc
	v_add_u32_e32 v6, 1, v2
	v_cmp_ge_u32_e32 vcc, v5, v3
	s_nop 1
	v_cndmask_b32_e32 v2, v2, v6, vcc
	v_mul_lo_u32 v5, v3, v2
	v_add_u32_e32 v3, v5, v3
	v_cmp_ne_u32_e32 vcc, v4, v3
	s_and_saveexec_b64 s[8:9], vcc
	s_xor_b64 s[8:9], exec, s[8:9]
	s_cbranch_execz .LBB0_1074
	s_waitcnt lgkmcnt(0)
	v_mov_b32_e32 v1, 0x3000
	global_load_dword v1, v1, s[4:5] offset:1280 sc1
	s_add_u32 s12, s4, 0x3500
	s_addc_u32 s13, s5, 0
	s_waitcnt vmcnt(0)
	v_cmp_eq_u32_e32 vcc, v1, v2
	s_and_saveexec_b64 s[10:11], vcc
	s_cbranch_execz .LBB0_1073
	s_mov_b32 s30, 1
	s_mov_b64 s[14:15], 0
	v_mov_b32_e32 v1, 0
	s_branch .LBB0_1064

; __device__ __forceinline__ unsigned xb_ld(unsigned* p)              { return __hip_atomic_load(p, __ATOMIC_RELAXED, __HIP_MEMORY_SCOPE_AGENT); }
; __device__ __forceinline__ unsigned xb_add(unsigned* p, unsigned v) { return __hip_atomic_fetch_add(p, v, __ATOMIC_RELAXED, __HIP_MEMORY_SCOPE_AGENT); }
; #define XB_SPIN(cond, bar) do { unsigned _sp = 0; while (cond) { __builtin_amdgcn_s_sleep(1); \
;     if ((++_sp & 255u) == 0u) { if (xb_ld(&(bar)[XB_TMO])) break; if (_sp > XB_SPIN_CAP) { atomicAdd(&(bar)[XB_TMO], 1u); break; } } } } while (0)
; __device__ __forceinline__ void xcd_barrier(const XcdBarrier& b) {
;     ...
;         if (old + 1u == (gen + 1u) * nloc) {
;             __builtin_amdgcn_fence(__ATOMIC_RELEASE, "agent");
;             asm volatile("s_waitcnt vmcnt(0)" ::: "memory");
;             const unsigned og = xb_add(&bar[XB_TOP], 1u);
;             const unsigned tg = og / nx;
;             if (og + 1u == (tg + 1u) * nx) xb_add(&bar[XB_TOPGEN], 1u);
;             else XB_SPIN(xb_ld(&bar[XB_TOPGEN]) == tg, bar);
;             __builtin_amdgcn_fence(__ATOMIC_ACQUIRE, "agent");
;             xb_add(&bar[XB_XGEN(b.x)], 1u);
;             asm volatile("s_waitcnt vmcnt(0)" ::: "memory");
.LBB0_1091:
	s_or_b64 exec, exec, s[4:5]
	v_mov_b32_e32 v1, 0x2000
	v_mov_b32_e32 v2, 1
	s_waitcnt vmcnt(0)
	buffer_inv sc1
	s_waitcnt vmcnt(0)

; __device__ __forceinline__ unsigned xb_ld(unsigned* p)              { return __hip_atomic_load(p, __ATOMIC_RELAXED, __HIP_MEMORY_SCOPE_AGENT); }
; __device__ __forceinline__ unsigned xb_add(unsigned* p, unsigned v) { return __hip_atomic_fetch_add(p, v, __ATOMIC_RELAXED, __HIP_MEMORY_SCOPE_AGENT); }
; #define XB_SPIN(cond, bar) do { unsigned _sp = 0; while (cond) { __builtin_amdgcn_s_sleep(1); \
;     if ((++_sp & 255u) == 0u) { if (xb_ld(&(bar)[XB_TMO])) break; if (_sp > XB_SPIN_CAP) { atomicAdd(&(bar)[XB_TMO], 1u); break; } } } } while (0)
; __device__ __forceinline__ void xcd_barrier(const XcdBarrier& b) {
;     ...
;         unsigned nloc = b.st[0], nx = b.st[1];
;         if (nloc == 0u) { xcd_barrier_complete(bar, b.x, nloc, nx); b.st[0] = nloc; b.st[1] = nx; }
;         const unsigned old = xb_add(&bar[XB_XSUB(b.x)], 1u);
;         const unsigned gen = old / nloc;
;         if (old + 1u == (gen + 1u) * nloc) {
;             __builtin_amdgcn_fence(__ATOMIC_RELEASE, "agent");
;             asm volatile("s_waitcnt vmcnt(0)" ::: "memory");
;             const unsigned og = xb_add(&bar[XB_TOP], 1u);
;             const unsigned tg = og / nx;
;             if (og + 1u == (tg + 1u) * nx) xb_add(&bar[XB_TOPGEN], 1u);
;             else XB_SPIN(xb_ld(&bar[XB_TOPGEN]) == tg, bar);
;             __builtin_amdgcn_fence(__ATOMIC_ACQUIRE, "agent");
;             xb_add(&bar[XB_XGEN(b.x)], 1u);
;             asm volatile("s_waitcnt vmcnt(0)" ::: "memory");
;         } else {
;             XB_SPIN(xb_ld(&bar[XB_XGEN(b.x)]) == gen, bar);
.LBB0_1168:
	v_readlane_b32 s4, v252, 35
	v_readlane_b32 s5, v252, 36
	s_lshl_b64 s[4:5], s[4:5], 2
	v_readlane_b32 s6, v252, 33
	s_add_u32 s6, s6, s4
	v_readlane_b32 s4, v252, 34
	s_addc_u32 s7, s4, s5
	v_readlane_b32 s4, v252, 37
	s_lshl_b32 s4, s4, 8
	s_add_u32 s4, s6, s4
	s_addc_u32 s5, s7, 0
	v_mov_b32_e32 v2, 0x1000
	v_mov_b32_e32 v4, 1
	global_atomic_add v4, v2, v4, s[4:5] offset:1024 sc0
	v_cvt_f32_u32_e32 v2, v3
	v_sub_u32_e32 v5, 0, v3
	v_rcp_iflag_f32_e32 v2, v2
	s_nop 0
	v_mul_f32_e32 v2, 0x4f7ffffe, v2
	v_cvt_u32_f32_e32 v2, v2
	v_mul_lo_u32 v5, v5, v2
	v_mul_hi_u32 v5, v2, v5
	v_add_u32_e32 v2, v2, v5
	s_waitcnt vmcnt(0)
	v_mul_hi_u32 v2, v4, v2
	v_mul_lo_u32 v5, v2, v3
	v_sub_u32_e32 v5, v4, v5
	v_add_u32_e32 v6, 1, v2
	v_cmp_ge_u32_e32 vcc, v5, v3
	v_add_u32_e32 v4, 1, v4
	s_nop 0
	v_cndmask_b32_e32 v2, v2, v6, vcc
	v_sub_u32_e32 v6, v5, v3
	v_cndmask_b32_e32 v5, v5, v6, vcc
	v_add_u32_e32 v6, 1, v2
	v_cmp_ge_u32_e32 vcc, v5, v3
	s_nop 1
	v_cndmask_b32_e32 v2, v2, v6, vcc
	v_mul_lo_u32 v5, v3, v2
	v_add_u32_e32 v3, v5, v3
	v_cmp_ne_u32_e32 vcc, v4, v3
	s_and_saveexec_b64 s[8:9], vcc
	s_xor_b64 s[8:9], exec, s[8:9]
	s_cbranch_execz .LBB0_1182
	s_waitcnt lgkmcnt(0)
	v_mov_b32_e32 v1, 0x3000
	global_load_dword v1, v1, s[6:7] offset:1280 sc1
	s_add_u32 s12, s6, 0x3500
	s_addc_u32 s13, s7, 0
	s_waitcnt vmcnt(0)
	v_cmp_eq_u32_e32 vcc, v1, v2
	s_and_saveexec_b64 s[10:11], vcc
	s_cbranch_execz .LBB0_1181
	s_mov_b32 s26, 1
	s_mov_b64 s[14:15], 0
	v_mov_b32_e32 v1, 0
	s_branch .LBB0_1172

; __device__ __forceinline__ unsigned xb_ld(unsigned* p)              { return __hip_atomic_load(p, __ATOMIC_RELAXED, __HIP_MEMORY_SCOPE_AGENT); }
; __device__ __forceinline__ unsigned xb_add(unsigned* p, unsigned v) { return __hip_atomic_fetch_add(p, v, __ATOMIC_RELAXED, __HIP_MEMORY_SCOPE_AGENT); }
; #define XB_SPIN(cond, bar) do { unsigned _sp = 0; while (cond) { __builtin_amdgcn_s_sleep(1); \
;     if ((++_sp & 255u) == 0u) { if (xb_ld(&(bar)[XB_TMO])) break; if (_sp > XB_SPIN_CAP) { atomicAdd(&(bar)[XB_TMO], 1u); break; } } } } while (0)
; __device__ __forceinline__ void xcd_barrier(const XcdBarrier& b) {
;     ...
;         unsigned nloc = b.st[0], nx = b.st[1];
;         if (nloc == 0u) { xcd_barrier_complete(bar, b.x, nloc, nx); b.st[0] = nloc; b.st[1] = nx; }
;         const unsigned old = xb_add(&bar[XB_XSUB(b.x)], 1u);
;         const unsigned gen = old / nloc;
;         if (old + 1u == (gen + 1u) * nloc) {
;             __builtin_amdgcn_fence(__ATOMIC_RELEASE, "agent");
;             asm volatile("s_waitcnt vmcnt(0)" ::: "memory");
;             const unsigned og = xb_add(&bar[XB_TOP], 1u);
;             const unsigned tg = og / nx;
;             if (og + 1u == (tg + 1u) * nx) xb_add(&bar[XB_TOPGEN], 1u);
;             else XB_SPIN(xb_ld(&bar[XB_TOPGEN]) == tg, bar);
;             __builtin_amdgcn_fence(__ATOMIC_ACQUIRE, "agent");
;             xb_add(&bar[XB_XGEN(b.x)], 1u);
;             asm volatile("s_waitcnt vmcnt(0)" ::: "memory");
;         } else {
;             XB_SPIN(xb_ld(&bar[XB_XGEN(b.x)]) == gen, bar);
.LBB0_1263:
	v_readlane_b32 s4, v252, 35
	v_readlane_b32 s5, v252, 36
	s_lshl_b64 s[4:5], s[4:5], 2
	v_readlane_b32 s6, v252, 33
	s_add_u32 s6, s6, s4
	v_readlane_b32 s4, v252, 34
	s_addc_u32 s7, s4, s5
	v_readlane_b32 s4, v252, 37
	s_lshl_b32 s4, s4, 8
	s_add_u32 s4, s6, s4
	s_addc_u32 s5, s7, 0
	v_mov_b32_e32 v2, 0x1000
	v_mov_b32_e32 v4, 1
	global_atomic_add v4, v2, v4, s[4:5] offset:1024 sc0
	v_cvt_f32_u32_e32 v2, v3
	v_sub_u32_e32 v5, 0, v3
	v_rcp_iflag_f32_e32 v2, v2
	s_nop 0
	v_mul_f32_e32 v2, 0x4f7ffffe, v2
	v_cvt_u32_f32_e32 v2, v2
	v_mul_lo_u32 v5, v5, v2
	v_mul_hi_u32 v5, v2, v5
	v_add_u32_e32 v2, v2, v5
	s_waitcnt vmcnt(0)
	v_mul_hi_u32 v2, v4, v2
	v_mul_lo_u32 v5, v2, v3
	v_sub_u32_e32 v5, v4, v5
	v_add_u32_e32 v6, 1, v2
	v_cmp_ge_u32_e32 vcc, v5, v3
	v_add_u32_e32 v4, 1, v4
	s_nop 0
	v_cndmask_b32_e32 v2, v2, v6, vcc
	v_sub_u32_e32 v6, v5, v3
	v_cndmask_b32_e32 v5, v5, v6, vcc
	v_add_u32_e32 v6, 1, v2
	v_cmp_ge_u32_e32 vcc, v5, v3
	s_nop 1
	v_cndmask_b32_e32 v2, v2, v6, vcc
	v_mul_lo_u32 v5, v3, v2
	v_add_u32_e32 v3, v5, v3
	v_cmp_ne_u32_e32 vcc, v4, v3
	s_and_saveexec_b64 s[8:9], vcc
	s_xor_b64 s[8:9], exec, s[8:9]
	s_cbranch_execz .LBB0_1277
	s_waitcnt lgkmcnt(0)
	v_mov_b32_e32 v1, 0x3000
	global_load_dword v1, v1, s[6:7] offset:1280 sc1
	s_add_u32 s12, s6, 0x3500
	s_addc_u32 s13, s7, 0
	s_waitcnt vmcnt(0)
	v_cmp_eq_u32_e32 vcc, v1, v2
	s_and_saveexec_b64 s[10:11], vcc
	s_cbranch_execz .LBB0_1276
	s_mov_b32 s33, 1
	s_mov_b64 s[22:23], 0
	v_mov_b32_e32 v1, 0
	s_branch .LBB0_1267
